# k73 plus hyena MFMA-loop LDS waits moved behind the four MFMAs of each step
# baseline (speedup 1.0000x reference)
; #define MFMA32(a, b, c) __builtin_amdgcn_mfma_f32_32x32x16_bf16((a), (b), (c), 0, 0, 0)
; #define HDSR(dst, addr, off) asm volatile("ds_read_b128 %0, %1 offset:%2" : "=v"(dst) : "v"(addr), "n"(off))
; #define HWAIT(a, b, c, d) asm volatile("s_waitcnt lgkmcnt(0)" : "+v"(a), "+v"(b), "+v"(c), "+v"(d))
; __device__ __forceinline__ void hyena_unit(KP Pk, Frame& F, int l, int cg) {
;     ...
; #pragma unroll 1
;                 for (int s0 = 0; s0 < nsteps; s0 += 6) {
;                     const unsigned an = apa - (unsigned)(s0 + 6) * 64u, bn = bpa - (unsigned)(s0 + 6) * 64u;
; #pragma unroll
;                     for (int j = 0; j < 6; ++j) if (s0 + j < nsteps) {
;                         if (s0 + j + 1 < nsteps) { HDSR(A2[(j + 1) & 1][0], an, (5 - j) * 64); HDSR(A2[(j + 1) & 1][1], an, (5 - j) * 64 + 32);
;                             HDSR(R[(j + 1) % 6][0], bn, (5 - j) * 64); HDSR(R[(j + 1) % 6][1], bn, (5 - j) * 64 + 32); }
;                         acc1 = MFMA32(A2[j & 1][0], R[(j + 2) % 6][0], acc1); acc0 = MFMA32(A2[j & 1][0], R[j][0], acc0);
;                         acc1 = MFMA32(A2[j & 1][1], R[(j + 2) % 6][1], acc1); acc0 = MFMA32(A2[j & 1][1], R[j][1], acc0);
;                         HWAIT(A2[(j + 1) & 1][0], A2[(j + 1) & 1][1], R[(j + 1) % 6][0], R[(j + 1) % 6][1]); }
;                 }
.LBB0_717:
	v_mfma_f32_32x32x16_bf16 v[16:31], v[64:67], v[56:59], v[16:31]
	v_mfma_f32_32x32x16_bf16 v[32:47], v[64:67], v[92:95], v[32:47]
	v_mfma_f32_32x32x16_bf16 v[16:31], v[68:71], v[60:63], v[16:31]
	v_mfma_f32_32x32x16_bf16 v[32:47], v[68:71], v[104:107], v[32:47]
	s_waitcnt lgkmcnt(0)

; #define MFMA32(a, b, c) __builtin_amdgcn_mfma_f32_32x32x16_bf16((a), (b), (c), 0, 0, 0)
; #define HDSR(dst, addr, off) asm volatile("ds_read_b128 %0, %1 offset:%2" : "=v"(dst) : "v"(addr), "n"(off))
; #define HWAIT(a, b, c, d) asm volatile("s_waitcnt lgkmcnt(0)" : "+v"(a), "+v"(b), "+v"(c), "+v"(d))
; __device__ __forceinline__ void hyena_unit(KP Pk, Frame& F, int l, int cg) {
;     ...
; #pragma unroll 1
;                 for (int s0 = 0; s0 < nsteps; s0 += 6) {
;                     const unsigned an = apa - (unsigned)(s0 + 6) * 64u, bn = bpa - (unsigned)(s0 + 6) * 64u;
; #pragma unroll
;                     for (int j = 0; j < 6; ++j) if (s0 + j < nsteps) {
;                         if (s0 + j + 1 < nsteps) { HDSR(A2[(j + 1) & 1][0], an, (5 - j) * 64); HDSR(A2[(j + 1) & 1][1], an, (5 - j) * 64 + 32);
;                             HDSR(R[(j + 1) % 6][0], bn, (5 - j) * 64); HDSR(R[(j + 1) % 6][1], bn, (5 - j) * 64 + 32); }
;                         acc1 = MFMA32(A2[j & 1][0], R[(j + 2) % 6][0], acc1); acc0 = MFMA32(A2[j & 1][0], R[j][0], acc0);
;                         acc1 = MFMA32(A2[j & 1][1], R[(j + 2) % 6][1], acc1); acc0 = MFMA32(A2[j & 1][1], R[j][1], acc0);
;                         HWAIT(A2[(j + 1) & 1][0], A2[(j + 1) & 1][1], R[(j + 1) % 6][0], R[(j + 1) % 6][1]); }
;                 }
.LBB0_727:
	v_mfma_f32_32x32x16_bf16 v[16:31], v[108:111], v[72:75], v[16:31]
	v_mfma_f32_32x32x16_bf16 v[32:47], v[108:111], v[100:103], v[32:47]
	v_mfma_f32_32x32x16_bf16 v[16:31], v[116:119], v[80:83], v[16:31]
	v_mfma_f32_32x32x16_bf16 v[32:47], v[116:119], v[112:115], v[32:47]
	s_waitcnt lgkmcnt(0)
	s_cmp_lt_i32 s60, s37
	s_cselect_b64 s[40:41], -1, 0
	s_cmp_ge_i32 s60, s37
	s_cbranch_scc1 .LBB0_721

; #define MFMA32(a, b, c) __builtin_amdgcn_mfma_f32_32x32x16_bf16((a), (b), (c), 0, 0, 0)
; #define HDSR(dst, addr, off) asm volatile("ds_read_b128 %0, %1 offset:%2" : "=v"(dst) : "v"(addr), "n"(off))
; #define HWAIT(a, b, c, d) asm volatile("s_waitcnt lgkmcnt(0)" : "+v"(a), "+v"(b), "+v"(c), "+v"(d))
; __device__ __forceinline__ void hyena_unit(KP Pk, Frame& F, int l, int cg) {
;     ...
; #pragma unroll 1
;                 for (int s0 = 0; s0 < nsteps; s0 += 6) {
;                     const unsigned an = apa - (unsigned)(s0 + 6) * 64u, bn = bpa - (unsigned)(s0 + 6) * 64u;
; #pragma unroll
;                     for (int j = 0; j < 6; ++j) if (s0 + j < nsteps) {
;                         if (s0 + j + 1 < nsteps) { HDSR(A2[(j + 1) & 1][0], an, (5 - j) * 64); HDSR(A2[(j + 1) & 1][1], an, (5 - j) * 64 + 32);
;                             HDSR(R[(j + 1) % 6][0], bn, (5 - j) * 64); HDSR(R[(j + 1) % 6][1], bn, (5 - j) * 64 + 32); }
;                         acc1 = MFMA32(A2[j & 1][0], R[(j + 2) % 6][0], acc1); acc0 = MFMA32(A2[j & 1][0], R[j][0], acc0);
;                         acc1 = MFMA32(A2[j & 1][1], R[(j + 2) % 6][1], acc1); acc0 = MFMA32(A2[j & 1][1], R[j][1], acc0);
;                         HWAIT(A2[(j + 1) & 1][0], A2[(j + 1) & 1][1], R[(j + 1) % 6][0], R[(j + 1) % 6][1]); }
;                 }
.LBB0_730:
	v_mfma_f32_32x32x16_bf16 v[16:31], v[64:67], v[76:79], v[16:31]
	v_mfma_f32_32x32x16_bf16 v[32:47], v[64:67], v[56:59], v[32:47]
	v_mfma_f32_32x32x16_bf16 v[16:31], v[68:71], v[88:91], v[16:31]
	v_mfma_f32_32x32x16_bf16 v[32:47], v[68:71], v[60:63], v[32:47]
	s_waitcnt lgkmcnt(0)
	s_andn2_b64 vcc, exec, s[40:41]
	s_cbranch_vccnz .LBB0_722

; #define MFMA32(a, b, c) __builtin_amdgcn_mfma_f32_32x32x16_bf16((a), (b), (c), 0, 0, 0)
; #define HDSR(dst, addr, off) asm volatile("ds_read_b128 %0, %1 offset:%2" : "=v"(dst) : "v"(addr), "n"(off))
; #define HWAIT(a, b, c, d) asm volatile("s_waitcnt lgkmcnt(0)" : "+v"(a), "+v"(b), "+v"(c), "+v"(d))
; __device__ __forceinline__ void hyena_unit(KP Pk, Frame& F, int l, int cg) {
;     ...
; #pragma unroll 1
;                 for (int s0 = 0; s0 < nsteps; s0 += 6) {
;                     const unsigned an = apa - (unsigned)(s0 + 6) * 64u, bn = bpa - (unsigned)(s0 + 6) * 64u;
; #pragma unroll
;                     for (int j = 0; j < 6; ++j) if (s0 + j < nsteps) {
;                         if (s0 + j + 1 < nsteps) { HDSR(A2[(j + 1) & 1][0], an, (5 - j) * 64); HDSR(A2[(j + 1) & 1][1], an, (5 - j) * 64 + 32);
;                             HDSR(R[(j + 1) % 6][0], bn, (5 - j) * 64); HDSR(R[(j + 1) % 6][1], bn, (5 - j) * 64 + 32); }
;                         acc1 = MFMA32(A2[j & 1][0], R[(j + 2) % 6][0], acc1); acc0 = MFMA32(A2[j & 1][0], R[j][0], acc0);
;                         acc1 = MFMA32(A2[j & 1][1], R[(j + 2) % 6][1], acc1); acc0 = MFMA32(A2[j & 1][1], R[j][1], acc0);
;                         HWAIT(A2[(j + 1) & 1][0], A2[(j + 1) & 1][1], R[(j + 1) % 6][0], R[(j + 1) % 6][1]); }
;                 }
.LBB0_733:
	v_mfma_f32_32x32x16_bf16 v[16:31], v[108:111], v[84:87], v[16:31]
	v_mfma_f32_32x32x16_bf16 v[32:47], v[108:111], v[72:75], v[32:47]
	v_mfma_f32_32x32x16_bf16 v[16:31], v[116:119], v[96:99], v[16:31]
	v_mfma_f32_32x32x16_bf16 v[32:47], v[116:119], v[80:83], v[32:47]
	s_waitcnt lgkmcnt(0)
	s_add_i32 s40, s60, 3
	s_cmp_gt_i32 s40, s37
	s_cbranch_scc1 .LBB0_723

; #define MFMA32(a, b, c) __builtin_amdgcn_mfma_f32_32x32x16_bf16((a), (b), (c), 0, 0, 0)
; #define HDSR(dst, addr, off) asm volatile("ds_read_b128 %0, %1 offset:%2" : "=v"(dst) : "v"(addr), "n"(off))
; #define HWAIT(a, b, c, d) asm volatile("s_waitcnt lgkmcnt(0)" : "+v"(a), "+v"(b), "+v"(c), "+v"(d))
; __device__ __forceinline__ void hyena_unit(KP Pk, Frame& F, int l, int cg) {
;     ...
; #pragma unroll 1
;                 for (int s0 = 0; s0 < nsteps; s0 += 6) {
;                     const unsigned an = apa - (unsigned)(s0 + 6) * 64u, bn = bpa - (unsigned)(s0 + 6) * 64u;
; #pragma unroll
;                     for (int j = 0; j < 6; ++j) if (s0 + j < nsteps) {
;                         if (s0 + j + 1 < nsteps) { HDSR(A2[(j + 1) & 1][0], an, (5 - j) * 64); HDSR(A2[(j + 1) & 1][1], an, (5 - j) * 64 + 32);
;                             HDSR(R[(j + 1) % 6][0], bn, (5 - j) * 64); HDSR(R[(j + 1) % 6][1], bn, (5 - j) * 64 + 32); }
;                         acc1 = MFMA32(A2[j & 1][0], R[(j + 2) % 6][0], acc1); acc0 = MFMA32(A2[j & 1][0], R[j][0], acc0);
;                         acc1 = MFMA32(A2[j & 1][1], R[(j + 2) % 6][1], acc1); acc0 = MFMA32(A2[j & 1][1], R[j][1], acc0);
;                         HWAIT(A2[(j + 1) & 1][0], A2[(j + 1) & 1][1], R[(j + 1) % 6][0], R[(j + 1) % 6][1]); }
;                 }
.LBB0_736:
	v_mfma_f32_32x32x16_bf16 v[16:31], v[64:67], v[92:95], v[16:31]
	v_mfma_f32_32x32x16_bf16 v[32:47], v[64:67], v[76:79], v[32:47]
	v_mfma_f32_32x32x16_bf16 v[16:31], v[68:71], v[104:107], v[16:31]
	v_mfma_f32_32x32x16_bf16 v[32:47], v[68:71], v[88:91], v[32:47]
	s_waitcnt lgkmcnt(0)
	s_add_i32 s40, s60, 4
	s_cmp_gt_i32 s40, s37
	s_cbranch_scc1 .LBB0_724

; #define MFMA32(a, b, c) __builtin_amdgcn_mfma_f32_32x32x16_bf16((a), (b), (c), 0, 0, 0)
; #define HDSR(dst, addr, off) asm volatile("ds_read_b128 %0, %1 offset:%2" : "=v"(dst) : "v"(addr), "n"(off))
; #define HWAIT(a, b, c, d) asm volatile("s_waitcnt lgkmcnt(0)" : "+v"(a), "+v"(b), "+v"(c), "+v"(d))
; __device__ __forceinline__ void hyena_unit(KP Pk, Frame& F, int l, int cg) {
;     ...
; #pragma unroll 1
;                 for (int s0 = 0; s0 < nsteps; s0 += 6) {
;                     const unsigned an = apa - (unsigned)(s0 + 6) * 64u, bn = bpa - (unsigned)(s0 + 6) * 64u;
; #pragma unroll
;                     for (int j = 0; j < 6; ++j) if (s0 + j < nsteps) {
;                         if (s0 + j + 1 < nsteps) { HDSR(A2[(j + 1) & 1][0], an, (5 - j) * 64); HDSR(A2[(j + 1) & 1][1], an, (5 - j) * 64 + 32);
;                             HDSR(R[(j + 1) % 6][0], bn, (5 - j) * 64); HDSR(R[(j + 1) % 6][1], bn, (5 - j) * 64 + 32); }
;                         acc1 = MFMA32(A2[j & 1][0], R[(j + 2) % 6][0], acc1); acc0 = MFMA32(A2[j & 1][0], R[j][0], acc0);
;                         acc1 = MFMA32(A2[j & 1][1], R[(j + 2) % 6][1], acc1); acc0 = MFMA32(A2[j & 1][1], R[j][1], acc0);
;                         HWAIT(A2[(j + 1) & 1][0], A2[(j + 1) & 1][1], R[(j + 1) % 6][0], R[(j + 1) % 6][1]); }
;                 }
.LBB0_739:
	v_mfma_f32_32x32x16_bf16 v[16:31], v[108:111], v[100:103], v[16:31]
	v_mfma_f32_32x32x16_bf16 v[32:47], v[108:111], v[84:87], v[32:47]
	v_mfma_f32_32x32x16_bf16 v[16:31], v[116:119], v[112:115], v[16:31]
	v_mfma_f32_32x32x16_bf16 v[32:47], v[116:119], v[96:99], v[32:47]
	s_waitcnt lgkmcnt(0)
	s_add_i32 s40, s60, 5
	s_cmp_gt_i32 s40, s37
	s_cbranch_scc1 .LBB0_718
